# attention step loops: output accumulator kept in place (removed per-step 32 v_mov_b64 + 64 v_mov_b32 register copies), on sc1/nt policy base
# speedup vs baseline: 1.0049x; 1.0049x over previous
.LBB0_677:
	v_mov_b32_e32 v232, v134
	v_mov_b32_e32 v231, v233
.LBB0_678:
	s_add_i32 s78, s80, 1
	s_add_i32 s72, s72, 1
	s_add_i32 s86, s86, 32
	s_add_i32 s87, s87, -1
	s_cmp_eq_u32 s72, 64
	s_cbranch_scc1 .LBB0_742

.LBB0_730:
	s_nop 6
	v_max_f32_e32 v66, v131, v131
	v_max_f32_e32 v67, v130, v130
	v_max_f32_e32 v66, v67, v66
	v_max3_f32 v66, v66, v132, v133
	v_max3_f32 v66, v66, v134, v135
	v_max3_f32 v66, v66, v136, v137
	v_and_b32_e32 v68, 64, v166
	v_max3_f32 v66, v66, v138, v139
	v_xor_b32_e32 v67, 32, v166
	v_add_u32_e32 v68, 64, v68
	v_max3_f32 v66, v66, v140, v141
	v_cmp_lt_i32_e32 vcc, v67, v68
	v_max3_f32 v66, v66, v142, v143
	v_max3_f32 v66, v66, v144, v145
	v_cndmask_b32_e32 v67, v166, v67, vcc
	v_lshlrev_b32_e32 v67, 2, v67
	ds_bpermute_b32 v67, v67, v66
	s_waitcnt lgkmcnt(0)
	v_max_f32_e32 v67, v67, v67
	v_max_f32_e32 v66, v66, v67
	v_add_f32_e32 v67, 0x40c00000, v231
	v_cmp_gt_f32_e32 vcc, v66, v67
	s_nop 1
	v_cndmask_b32_e32 v233, v231, v66, vcc
	v_sub_f32_e32 v66, v231, v233
	v_exp_f32_e32 v146, v66
	s_cbranch_vccz .LBB0_732
	v_pk_mul_f32 v[64:65], v[64:65], v[146:147] op_sel_hi:[1,0]
	v_pk_mul_f32 v[62:63], v[62:63], v[146:147] op_sel_hi:[1,0]
	v_pk_mul_f32 v[60:61], v[60:61], v[146:147] op_sel_hi:[1,0]
	v_pk_mul_f32 v[58:59], v[58:59], v[146:147] op_sel_hi:[1,0]
	v_pk_mul_f32 v[56:57], v[56:57], v[146:147] op_sel_hi:[1,0]
	v_pk_mul_f32 v[54:55], v[54:55], v[146:147] op_sel_hi:[1,0]
	v_pk_mul_f32 v[52:53], v[52:53], v[146:147] op_sel_hi:[1,0]
	v_pk_mul_f32 v[50:51], v[50:51], v[146:147] op_sel_hi:[1,0]
	v_pk_mul_f32 v[48:49], v[48:49], v[146:147] op_sel_hi:[1,0]
	v_pk_mul_f32 v[46:47], v[46:47], v[146:147] op_sel_hi:[1,0]
	v_pk_mul_f32 v[44:45], v[44:45], v[146:147] op_sel_hi:[1,0]
	v_pk_mul_f32 v[42:43], v[42:43], v[146:147] op_sel_hi:[1,0]
	v_pk_mul_f32 v[40:41], v[40:41], v[146:147] op_sel_hi:[1,0]
	v_pk_mul_f32 v[38:39], v[38:39], v[146:147] op_sel_hi:[1,0]
	v_pk_mul_f32 v[36:37], v[36:37], v[146:147] op_sel_hi:[1,0]
	v_pk_mul_f32 v[34:35], v[34:35], v[146:147] op_sel_hi:[1,0]
	v_pk_mul_f32 v[32:33], v[32:33], v[146:147] op_sel_hi:[1,0]
	v_pk_mul_f32 v[30:31], v[30:31], v[146:147] op_sel_hi:[1,0]
	v_pk_mul_f32 v[28:29], v[28:29], v[146:147] op_sel_hi:[1,0]
	v_pk_mul_f32 v[26:27], v[26:27], v[146:147] op_sel_hi:[1,0]
	v_pk_mul_f32 v[24:25], v[24:25], v[146:147] op_sel_hi:[1,0]
	v_pk_mul_f32 v[22:23], v[22:23], v[146:147] op_sel_hi:[1,0]
	v_pk_mul_f32 v[20:21], v[20:21], v[146:147] op_sel_hi:[1,0]
	v_pk_mul_f32 v[18:19], v[18:19], v[146:147] op_sel_hi:[1,0]
	v_pk_mul_f32 v[16:17], v[16:17], v[146:147] op_sel_hi:[1,0]
	v_pk_mul_f32 v[14:15], v[14:15], v[146:147] op_sel_hi:[1,0]
	v_pk_mul_f32 v[12:13], v[12:13], v[146:147] op_sel_hi:[1,0]
	v_pk_mul_f32 v[10:11], v[10:11], v[146:147] op_sel_hi:[1,0]
	v_pk_mul_f32 v[8:9], v[8:9], v[146:147] op_sel_hi:[1,0]
	v_pk_mul_f32 v[6:7], v[6:7], v[146:147] op_sel_hi:[1,0]
	v_pk_mul_f32 v[4:5], v[4:5], v[146:147] op_sel_hi:[1,0]
	v_pk_mul_f32 v[2:3], v[2:3], v[146:147] op_sel_hi:[1,0]
	s_branch .LBB0_733
.LBB0_732:
.LBB0_733:
	v_sub_f32_e32 v130, v130, v233
	v_exp_f32_e32 v130, v130
	v_sub_f32_e32 v131, v131, v233
	v_exp_f32_e32 v131, v131
	v_sub_f32_e32 v132, v132, v233
	v_exp_f32_e32 v132, v132
	v_sub_f32_e32 v133, v133, v233
	v_exp_f32_e32 v133, v133
	v_sub_f32_e32 v134, v134, v233
	v_add_f32_e32 v220, 0, v130
	v_exp_f32_e32 v221, v134
	v_add_f32_e32 v220, v131, v220
	v_add_f32_e32 v220, v132, v220
	v_sub_f32_e32 v135, v135, v233
	v_add_f32_e32 v220, v133, v220
	v_exp_f32_e32 v135, v135
	v_sub_f32_e32 v136, v136, v233
	v_add_f32_e32 v134, v221, v220
	v_exp_f32_e32 v220, v136
	v_sub_f32_e32 v136, v137, v233
	v_exp_f32_e32 v222, v136
	v_sub_f32_e32 v136, v138, v233
	v_exp_f32_e32 v223, v136
	v_sub_f32_e32 v136, v139, v233
	v_add_f32_e32 v134, v135, v134
	v_exp_f32_e32 v234, v136
	v_sub_f32_e32 v136, v140, v233
	v_add_f32_e32 v134, v220, v134
	v_exp_f32_e32 v140, v136
	v_sub_f32_e32 v136, v141, v233
	v_add_f32_e32 v134, v222, v134
	v_exp_f32_e32 v141, v136
	v_sub_f32_e32 v136, v142, v233
	v_add_f32_e32 v134, v223, v134
	v_exp_f32_e32 v142, v136
	v_sub_f32_e32 v136, v143, v233
	v_add_f32_e32 v134, v234, v134
	v_exp_f32_e32 v143, v136
	v_sub_f32_e32 v136, v144, v233
	v_add_f32_e32 v134, v140, v134
	v_exp_f32_e32 v144, v136
	v_sub_f32_e32 v136, v145, v233
	v_add_f32_e32 v134, v141, v134
	v_exp_f32_e32 v145, v136
	v_add_f32_e32 v134, v142, v134
	v_add_f32_e32 v134, v143, v134
	v_add_f32_e32 v134, v144, v134
	v_add_f32_e32 v134, v145, v134
	v_cvt_pk_bf16_f32 v136, v130, v131
	v_cvt_pk_bf16_f32 v137, v132, v133
	v_cvt_pk_bf16_f32 v138, v221, v135
	v_cvt_pk_bf16_f32 v139, v220, v222
	v_cvt_pk_bf16_f32 v130, v223, v234
	v_cvt_pk_bf16_f32 v131, v140, v141
	v_cvt_pk_bf16_f32 v132, v142, v143
	v_cvt_pk_bf16_f32 v133, v144, v145
	v_add_u32_e32 v135, s80, v184
	v_add_u32_e32 v144, s80, v185
	v_add_u32_e32 v145, s80, v187
	v_fmac_f32_e32 v134, v232, v146
	v_add3_u32 v140, v144, v186, v173
	v_add3_u32 v142, v145, v188, v173
	v_add3_u32 v146, v135, v186, v173
	ds_read_b64_tr_b16 v[140:141], v140 offset:8192
	ds_read_b64_tr_b16 v[142:143], v142 offset:8192
	ds_read_b64_tr_b16 v[234:235], v146 offset:8192
	v_add_u32_e32 v146, s80, v189
	v_add3_u32 v220, v146, v190, v173
	ds_read_b64_tr_b16 v[236:237], v220 offset:8192
	v_add3_u32 v220, v144, v191, v173
	ds_read_b64_tr_b16 v[238:239], v220 offset:8192
	v_add3_u32 v220, v145, v192, v173
	ds_read_b64_tr_b16 v[240:241], v220 offset:8192
	v_add3_u32 v220, v135, v191, v173
	ds_read_b64_tr_b16 v[242:243], v220 offset:8192
	v_add3_u32 v220, v146, v193, v173
	ds_read_b64_tr_b16 v[244:245], v220 offset:8192
	s_waitcnt lgkmcnt(6)
	v_mfma_f32_32x32x16_bf16 v[50:65], v[140:143], v[136:139], v[50:65]
	v_add3_u32 v140, v144, v194, v173
	v_add3_u32 v220, v135, v194, v173
	v_add3_u32 v144, v144, v197, v173
	v_add3_u32 v135, v135, v197, v173
	ds_read_b64_tr_b16 v[140:141], v140 offset:8192
	v_add3_u32 v142, v145, v195, v173
	ds_read_b64_tr_b16 v[142:143], v142 offset:8192
	s_waitcnt lgkmcnt(4)
	v_mfma_f32_32x32x16_bf16 v[34:49], v[238:241], v[136:139], v[34:49]
	ds_read_b64_tr_b16 v[238:239], v144 offset:8192
	v_add3_u32 v144, v145, v198, v173
	ds_read_b64_tr_b16 v[240:241], v144 offset:8192
	v_mfma_f32_32x32x16_bf16 v[50:65], v[234:237], v[130:133], v[50:65]
	ds_read_b64_tr_b16 v[234:235], v220 offset:8192
	v_add3_u32 v220, v146, v196, v173
	ds_read_b64_tr_b16 v[236:237], v220 offset:8192
	s_waitcnt lgkmcnt(6)
	v_mfma_f32_32x32x16_bf16 v[34:49], v[242:245], v[130:133], v[34:49]
	ds_read_b64_tr_b16 v[242:243], v135 offset:8192
	v_add3_u32 v135, v146, v199, v173
	ds_read_b64_tr_b16 v[244:245], v135 offset:8192
	s_waitcnt lgkmcnt(6)
	v_mfma_f32_32x32x16_bf16 v[18:33], v[140:143], v[136:139], v[18:33]
	s_and_b64 s[80:81], s[84:85], exec
	s_cselect_b32 s80, 0, s78
	s_mov_b64 s[84:85], 0
	s_waitcnt lgkmcnt(4)
	v_mfma_f32_32x32x16_bf16 v[2:17], v[238:241], v[136:139], v[2:17]
	s_waitcnt lgkmcnt(2)
	v_mfma_f32_32x32x16_bf16 v[18:33], v[234:237], v[130:133], v[18:33]
	s_waitcnt lgkmcnt(0)
	v_mfma_f32_32x32x16_bf16 v[2:17], v[242:245], v[130:133], v[2:17]

.LBB0_747:
	v_mov_b32_e32 v234, v134
	v_mov_b32_e32 v233, v235
.LBB0_748:
	s_add_i32 s78, s80, 1
	s_add_i32 s87, s87, 1
	s_add_i32 s86, s86, 32
	s_add_i32 s72, s72, -1
	s_cmp_eq_u32 s87, 64
	s_cbranch_scc1 .LBB0_812

.LBB0_800:
	s_nop 6
	v_max_f32_e32 v66, v131, v131
	v_max_f32_e32 v67, v130, v130
	v_max_f32_e32 v66, v67, v66
	v_max3_f32 v66, v66, v132, v133
	v_max3_f32 v66, v66, v134, v135
	v_max3_f32 v66, v66, v136, v137
	v_and_b32_e32 v68, 64, v166
	v_max3_f32 v66, v66, v138, v139
	v_xor_b32_e32 v67, 32, v166
	v_add_u32_e32 v68, 64, v68
	v_max3_f32 v66, v66, v140, v141
	v_cmp_lt_i32_e32 vcc, v67, v68
	v_max3_f32 v66, v66, v142, v143
	v_max3_f32 v66, v66, v144, v145
	v_cndmask_b32_e32 v67, v166, v67, vcc
	v_lshlrev_b32_e32 v67, 2, v67
	ds_bpermute_b32 v67, v67, v66
	s_waitcnt lgkmcnt(0)
	v_max_f32_e32 v67, v67, v67
	v_max_f32_e32 v66, v66, v67
	v_add_f32_e32 v67, 0x40c00000, v233
	v_cmp_gt_f32_e32 vcc, v66, v67
	s_nop 1
	v_cndmask_b32_e32 v235, v233, v66, vcc
	v_sub_f32_e32 v66, v233, v235
	v_exp_f32_e32 v146, v66
	s_cbranch_vccz .LBB0_802
	v_pk_mul_f32 v[64:65], v[64:65], v[146:147] op_sel_hi:[1,0]
	v_pk_mul_f32 v[62:63], v[62:63], v[146:147] op_sel_hi:[1,0]
	v_pk_mul_f32 v[60:61], v[60:61], v[146:147] op_sel_hi:[1,0]
	v_pk_mul_f32 v[58:59], v[58:59], v[146:147] op_sel_hi:[1,0]
	v_pk_mul_f32 v[56:57], v[56:57], v[146:147] op_sel_hi:[1,0]
	v_pk_mul_f32 v[54:55], v[54:55], v[146:147] op_sel_hi:[1,0]
	v_pk_mul_f32 v[52:53], v[52:53], v[146:147] op_sel_hi:[1,0]
	v_pk_mul_f32 v[50:51], v[50:51], v[146:147] op_sel_hi:[1,0]
	v_pk_mul_f32 v[48:49], v[48:49], v[146:147] op_sel_hi:[1,0]
	v_pk_mul_f32 v[46:47], v[46:47], v[146:147] op_sel_hi:[1,0]
	v_pk_mul_f32 v[44:45], v[44:45], v[146:147] op_sel_hi:[1,0]
	v_pk_mul_f32 v[42:43], v[42:43], v[146:147] op_sel_hi:[1,0]
	v_pk_mul_f32 v[40:41], v[40:41], v[146:147] op_sel_hi:[1,0]
	v_pk_mul_f32 v[38:39], v[38:39], v[146:147] op_sel_hi:[1,0]
	v_pk_mul_f32 v[36:37], v[36:37], v[146:147] op_sel_hi:[1,0]
	v_pk_mul_f32 v[34:35], v[34:35], v[146:147] op_sel_hi:[1,0]
	v_pk_mul_f32 v[32:33], v[32:33], v[146:147] op_sel_hi:[1,0]
	v_pk_mul_f32 v[30:31], v[30:31], v[146:147] op_sel_hi:[1,0]
	v_pk_mul_f32 v[28:29], v[28:29], v[146:147] op_sel_hi:[1,0]
	v_pk_mul_f32 v[26:27], v[26:27], v[146:147] op_sel_hi:[1,0]
	v_pk_mul_f32 v[24:25], v[24:25], v[146:147] op_sel_hi:[1,0]
	v_pk_mul_f32 v[22:23], v[22:23], v[146:147] op_sel_hi:[1,0]
	v_pk_mul_f32 v[20:21], v[20:21], v[146:147] op_sel_hi:[1,0]
	v_pk_mul_f32 v[18:19], v[18:19], v[146:147] op_sel_hi:[1,0]
	v_pk_mul_f32 v[16:17], v[16:17], v[146:147] op_sel_hi:[1,0]
	v_pk_mul_f32 v[14:15], v[14:15], v[146:147] op_sel_hi:[1,0]
	v_pk_mul_f32 v[12:13], v[12:13], v[146:147] op_sel_hi:[1,0]
	v_pk_mul_f32 v[10:11], v[10:11], v[146:147] op_sel_hi:[1,0]
	v_pk_mul_f32 v[8:9], v[8:9], v[146:147] op_sel_hi:[1,0]
	v_pk_mul_f32 v[6:7], v[6:7], v[146:147] op_sel_hi:[1,0]
	v_pk_mul_f32 v[4:5], v[4:5], v[146:147] op_sel_hi:[1,0]
	v_pk_mul_f32 v[2:3], v[2:3], v[146:147] op_sel_hi:[1,0]
	s_branch .LBB0_803
.LBB0_802:
.LBB0_803:
	v_sub_f32_e32 v130, v130, v235
	v_exp_f32_e32 v130, v130
	v_sub_f32_e32 v131, v131, v235
	v_exp_f32_e32 v131, v131
	v_sub_f32_e32 v132, v132, v235
	v_exp_f32_e32 v132, v132
	v_sub_f32_e32 v133, v133, v235
	v_exp_f32_e32 v133, v133
	v_sub_f32_e32 v134, v134, v235
	v_add_f32_e32 v220, 0, v130
	v_exp_f32_e32 v221, v134
	v_add_f32_e32 v220, v131, v220
	v_add_f32_e32 v220, v132, v220
	v_sub_f32_e32 v135, v135, v235
	v_add_f32_e32 v220, v133, v220
	v_exp_f32_e32 v135, v135
	v_sub_f32_e32 v136, v136, v235
	v_add_f32_e32 v134, v221, v220
	v_exp_f32_e32 v220, v136
	v_sub_f32_e32 v136, v137, v235
	v_exp_f32_e32 v222, v136
	v_sub_f32_e32 v136, v138, v235
	v_exp_f32_e32 v223, v136
	v_sub_f32_e32 v136, v139, v235
	v_add_f32_e32 v134, v135, v134
	v_exp_f32_e32 v236, v136
	v_sub_f32_e32 v136, v140, v235
	v_add_f32_e32 v134, v220, v134
	v_exp_f32_e32 v140, v136
	v_sub_f32_e32 v136, v141, v235
	v_add_f32_e32 v134, v222, v134
	v_exp_f32_e32 v141, v136
	v_sub_f32_e32 v136, v142, v235
	v_add_f32_e32 v134, v223, v134
	v_exp_f32_e32 v142, v136
	v_sub_f32_e32 v136, v143, v235
	v_add_f32_e32 v134, v236, v134
	v_exp_f32_e32 v143, v136
	v_sub_f32_e32 v136, v144, v235
	v_add_f32_e32 v134, v140, v134
	v_exp_f32_e32 v144, v136
	v_sub_f32_e32 v136, v145, v235
	v_add_f32_e32 v134, v141, v134
	v_exp_f32_e32 v145, v136
	v_add_f32_e32 v134, v142, v134
	v_add_f32_e32 v134, v143, v134
	v_add_f32_e32 v134, v144, v134
	v_add_f32_e32 v134, v145, v134
	v_cvt_pk_bf16_f32 v136, v130, v131
	v_cvt_pk_bf16_f32 v137, v132, v133
	v_cvt_pk_bf16_f32 v138, v221, v135
	v_cvt_pk_bf16_f32 v139, v220, v222
	v_cvt_pk_bf16_f32 v130, v223, v236
	v_cvt_pk_bf16_f32 v131, v140, v141
	v_cvt_pk_bf16_f32 v132, v142, v143
	v_cvt_pk_bf16_f32 v133, v144, v145
	v_add_u32_e32 v135, s80, v184
	v_add_u32_e32 v144, s80, v185
	v_add_u32_e32 v145, s80, v187
	v_fmac_f32_e32 v134, v234, v146
	v_add3_u32 v140, v144, v186, v173
	v_add3_u32 v142, v145, v188, v173
	v_add3_u32 v146, v135, v186, v173
	ds_read_b64_tr_b16 v[140:141], v140 offset:8192
	ds_read_b64_tr_b16 v[142:143], v142 offset:8192
	ds_read_b64_tr_b16 v[236:237], v146 offset:8192
	v_add_u32_e32 v146, s80, v189
	v_add3_u32 v220, v146, v190, v173
	ds_read_b64_tr_b16 v[238:239], v220 offset:8192
	v_add3_u32 v220, v144, v191, v173
	ds_read_b64_tr_b16 v[240:241], v220 offset:8192
	v_add3_u32 v220, v145, v192, v173
	ds_read_b64_tr_b16 v[242:243], v220 offset:8192
	v_add3_u32 v220, v135, v191, v173
	ds_read_b64_tr_b16 v[244:245], v220 offset:8192
	v_add3_u32 v220, v146, v193, v173
	ds_read_b64_tr_b16 v[246:247], v220 offset:8192
	s_waitcnt lgkmcnt(6)
	v_mfma_f32_32x32x16_bf16 v[50:65], v[140:143], v[136:139], v[50:65]
	v_add3_u32 v140, v144, v194, v173
	v_add3_u32 v220, v135, v194, v173
	v_add3_u32 v144, v144, v197, v173
	v_add3_u32 v135, v135, v197, v173
	ds_read_b64_tr_b16 v[140:141], v140 offset:8192
	v_add3_u32 v142, v145, v195, v173
	ds_read_b64_tr_b16 v[142:143], v142 offset:8192
	s_waitcnt lgkmcnt(4)
	v_mfma_f32_32x32x16_bf16 v[34:49], v[240:243], v[136:139], v[34:49]
	ds_read_b64_tr_b16 v[240:241], v144 offset:8192
	v_add3_u32 v144, v145, v198, v173
	ds_read_b64_tr_b16 v[242:243], v144 offset:8192
	v_mfma_f32_32x32x16_bf16 v[50:65], v[236:239], v[130:133], v[50:65]
	ds_read_b64_tr_b16 v[236:237], v220 offset:8192
	v_add3_u32 v220, v146, v196, v173
	ds_read_b64_tr_b16 v[238:239], v220 offset:8192
	s_waitcnt lgkmcnt(6)
	v_mfma_f32_32x32x16_bf16 v[34:49], v[244:247], v[130:133], v[34:49]
	ds_read_b64_tr_b16 v[244:245], v135 offset:8192
	v_add3_u32 v135, v146, v199, v173
	ds_read_b64_tr_b16 v[246:247], v135 offset:8192
	s_waitcnt lgkmcnt(6)
	v_mfma_f32_32x32x16_bf16 v[18:33], v[140:143], v[136:139], v[18:33]
	s_and_b64 s[80:81], s[84:85], exec
	s_cselect_b32 s80, 0, s78
	s_mov_b64 s[84:85], 0
	s_waitcnt lgkmcnt(4)
	v_mfma_f32_32x32x16_bf16 v[2:17], v[240:243], v[136:139], v[2:17]
	s_waitcnt lgkmcnt(2)
	v_mfma_f32_32x32x16_bf16 v[18:33], v[236:239], v[130:133], v[18:33]
	s_waitcnt lgkmcnt(0)
	v_mfma_f32_32x32x16_bf16 v[2:17], v[244:247], v[130:133], v[2:17]

.LBB0_817:
	v_mov_b32_e32 v234, v134
	v_mov_b32_e32 v233, v235
.LBB0_818:
	s_add_i32 s79, s81, 1
	s_add_i32 s73, s73, 1
	s_add_i32 s72, s72, 64
	s_add_i32 s86, s86, 32
	s_add_i32 s87, s87, -1
	s_cmp_eq_u32 s73, 64
	s_cbranch_scc1 .LBB0_882

.LBB0_872:
.LBB0_873:
	v_sub_f32_e32 v130, v130, v235
	v_exp_f32_e32 v130, v130
	v_sub_f32_e32 v131, v131, v235
	v_exp_f32_e32 v131, v131
	v_sub_f32_e32 v132, v132, v235
	v_exp_f32_e32 v132, v132
	v_sub_f32_e32 v133, v133, v235
	v_exp_f32_e32 v133, v133
	v_sub_f32_e32 v134, v134, v235
	v_add_f32_e32 v220, 0, v130
	v_exp_f32_e32 v221, v134
	v_add_f32_e32 v220, v131, v220
	v_add_f32_e32 v220, v132, v220
	v_sub_f32_e32 v135, v135, v235
	v_add_f32_e32 v220, v133, v220
	v_exp_f32_e32 v135, v135
	v_sub_f32_e32 v136, v136, v235
	v_add_f32_e32 v134, v221, v220
	v_exp_f32_e32 v220, v136
	v_sub_f32_e32 v136, v137, v235
	v_exp_f32_e32 v222, v136
	v_sub_f32_e32 v136, v138, v235
	v_exp_f32_e32 v223, v136
	v_sub_f32_e32 v136, v139, v235
	v_add_f32_e32 v134, v135, v134
	v_exp_f32_e32 v236, v136
	v_sub_f32_e32 v136, v140, v235
	v_add_f32_e32 v134, v220, v134
	v_exp_f32_e32 v140, v136
	v_sub_f32_e32 v136, v141, v235
	v_add_f32_e32 v134, v222, v134
	v_exp_f32_e32 v141, v136
	v_sub_f32_e32 v136, v142, v235
	v_add_f32_e32 v134, v223, v134
	v_exp_f32_e32 v142, v136
	v_sub_f32_e32 v136, v143, v235
	v_add_f32_e32 v134, v236, v134
	v_exp_f32_e32 v143, v136
	v_sub_f32_e32 v136, v144, v235
	v_add_f32_e32 v134, v140, v134
	v_exp_f32_e32 v144, v136
	v_sub_f32_e32 v136, v145, v235
	v_add_f32_e32 v134, v141, v134
	v_exp_f32_e32 v145, v136
	v_add_f32_e32 v134, v142, v134
	v_add_f32_e32 v134, v143, v134
	v_add_f32_e32 v134, v144, v134
	v_add_f32_e32 v134, v145, v134
	v_cvt_pk_bf16_f32 v136, v130, v131
	v_cvt_pk_bf16_f32 v137, v132, v133
	v_cvt_pk_bf16_f32 v138, v221, v135
	v_cvt_pk_bf16_f32 v139, v220, v222
	v_cvt_pk_bf16_f32 v130, v223, v236
	v_cvt_pk_bf16_f32 v131, v140, v141
	v_cvt_pk_bf16_f32 v132, v142, v143
	v_cvt_pk_bf16_f32 v133, v144, v145
	v_add_u32_e32 v135, s81, v184
	v_add_u32_e32 v144, s81, v185
	v_add_u32_e32 v145, s81, v187
	v_fmac_f32_e32 v134, v234, v146
	v_add3_u32 v140, v144, v186, v173
	v_add3_u32 v142, v145, v188, v173
	v_add3_u32 v146, v135, v186, v173
	ds_read_b64_tr_b16 v[140:141], v140 offset:8192
	ds_read_b64_tr_b16 v[142:143], v142 offset:8192
	ds_read_b64_tr_b16 v[236:237], v146 offset:8192
	v_add_u32_e32 v146, s81, v189
	v_add3_u32 v220, v146, v190, v173
	ds_read_b64_tr_b16 v[238:239], v220 offset:8192
	v_add3_u32 v220, v144, v191, v173
	ds_read_b64_tr_b16 v[240:241], v220 offset:8192
	v_add3_u32 v220, v145, v192, v173
	ds_read_b64_tr_b16 v[242:243], v220 offset:8192
	v_add3_u32 v220, v135, v191, v173
	ds_read_b64_tr_b16 v[244:245], v220 offset:8192
	v_add3_u32 v220, v146, v193, v173
	ds_read_b64_tr_b16 v[246:247], v220 offset:8192
	s_waitcnt lgkmcnt(6)
	v_mfma_f32_32x32x16_bf16 v[50:65], v[140:143], v[136:139], v[50:65]
	v_add3_u32 v140, v144, v194, v173
	v_add3_u32 v220, v135, v194, v173
	v_add3_u32 v144, v144, v197, v173
	v_add3_u32 v135, v135, v197, v173
	ds_read_b64_tr_b16 v[140:141], v140 offset:8192
	v_add3_u32 v142, v145, v195, v173
	ds_read_b64_tr_b16 v[142:143], v142 offset:8192
	s_waitcnt lgkmcnt(4)
	v_mfma_f32_32x32x16_bf16 v[34:49], v[240:243], v[136:139], v[34:49]
	ds_read_b64_tr_b16 v[240:241], v144 offset:8192
	v_add3_u32 v144, v145, v198, v173
	ds_read_b64_tr_b16 v[242:243], v144 offset:8192
	v_mfma_f32_32x32x16_bf16 v[50:65], v[236:239], v[130:133], v[50:65]
	ds_read_b64_tr_b16 v[236:237], v220 offset:8192
	v_add3_u32 v220, v146, v196, v173
	ds_read_b64_tr_b16 v[238:239], v220 offset:8192
	s_waitcnt lgkmcnt(6)
	v_mfma_f32_32x32x16_bf16 v[34:49], v[244:247], v[130:133], v[34:49]
	ds_read_b64_tr_b16 v[244:245], v135 offset:8192
	v_add3_u32 v135, v146, v199, v173
	ds_read_b64_tr_b16 v[246:247], v135 offset:8192
	s_waitcnt lgkmcnt(6)
	v_mfma_f32_32x32x16_bf16 v[18:33], v[140:143], v[136:139], v[18:33]
	s_and_b64 s[84:85], s[84:85], exec
	s_cselect_b32 s81, 0, s79
	s_mov_b64 s[84:85], 0
	s_waitcnt lgkmcnt(4)
	v_mfma_f32_32x32x16_bf16 v[2:17], v[240:243], v[136:139], v[2:17]
	s_waitcnt lgkmcnt(2)
	v_mfma_f32_32x32x16_bf16 v[18:33], v[236:239], v[130:133], v[18:33]
	s_waitcnt lgkmcnt(0)
	v_mfma_f32_32x32x16_bf16 v[2:17], v[244:247], v[130:133], v[2:17]
